# speedup vs baseline: 1.0063x; 1.0063x over previous
_Z9l1_kernelPKiS0_P15HIP_vector_typeIjLj2EEPiS4_PKfS6_S6_S6_PfP6__half:
	s_cmp_gt_u32 s2, 42
	s_mov_b64 s[4:5], -1
	s_cbranch_scc0 .LBB0_17
	s_mul_i32 s15, s2, 0xeb
	s_add_i32 s3, s15, 0xffffd887
	s_min_i32 s16, s3, 0xc265
	s_add_i32 s12, s16, 0xeb
	s_cmp_ge_i32 s3, s12
	s_cbranch_scc1 .LBB0_16
	s_load_dwordx4 s[4:7], s[0:1], 0x28
	s_load_dwordx2 s[10:11], s[0:1], 0x38
	v_lshlrev_b32_e32 v1, 4, v0
	v_and_b32_e32 v2, 0x1f0, v1
	v_mov_b32_e32 v3, 0
	v_lshrrev_b32_e32 v1, 5, v0
	s_add_i32 s13, s16, 0xea
	s_waitcnt lgkmcnt(0)
	v_lshl_add_u64 v[110:111], s[4:5], 0, v[2:3]
	v_add_u32_e32 v2, s3, v1
	v_min_i32_e32 v2, s13, v2
	v_ashrrev_i32_e32 v3, 31, v2
	v_lshlrev_b64 v[2:3], 9, v[2:3]
	v_lshl_add_u64 v[10:11], v[110:111], 0, v[2:3]
	v_or_b32_e32 v2, 0x200, v0
	v_lshrrev_b32_e32 v146, 5, v2
	v_add_u32_e32 v2, s3, v146
	v_min_i32_e32 v2, s13, v2
	v_ashrrev_i32_e32 v3, 31, v2
	v_lshlrev_b64 v[2:3], 9, v[2:3]
	v_or_b32_e32 v147, 32, v1
	v_lshl_add_u64 v[12:13], v[110:111], 0, v[2:3]
	global_load_dwordx4 v[2:5], v[10:11], off
	global_load_dwordx4 v[6:9], v[12:13], off
	v_add_u32_e32 v10, s3, v147
	v_min_i32_e32 v10, s13, v10
	v_ashrrev_i32_e32 v11, 31, v10
	v_lshlrev_b64 v[10:11], 9, v[10:11]
	v_lshl_add_u64 v[10:11], v[110:111], 0, v[10:11]
	global_load_dwordx4 v[10:13], v[10:11], off
	v_lshrrev_b32_e32 v149, 6, v0
	s_movk_i32 s4, 0x200
	v_and_b32_e32 v150, 15, v0
	v_cmp_gt_u32_e32 vcc, s4, v0
	v_lshlrev_b32_e32 v151, 4, v149
	s_and_saveexec_b64 s[4:5], vcc
	s_xor_b64 s[4:5], exec, s[4:5]
	v_or_b32_e32 v32, v151, v150
	s_or_saveexec_b64 s[4:5], s[4:5]
	v_lshlrev_b32_e32 v14, 1, v150
	v_mov_b64_e32 v[30:31], s[6:7]
	s_xor_b64 exec, exec, s[4:5]
	v_and_b32_e32 v15, 0x60, v151
	v_bfe_u32 v16, v0, 6, 1
	v_or3_b32 v32, v16, v15, v14
	v_mov_b64_e32 v[30:31], s[10:11]
	s_or_b64 exec, exec, s[4:5]
	s_movk_i32 s17, 0x110
	s_mov_b32 s14, 0x7060302
	s_sub_i32 s19, s16, s3
	s_addk_i32 s19, 0x11a
	s_load_dwordx4 s[24:27], s[0:1], 0x40
	s_load_dwordx2 s[28:29], s[0:1], 0x50
	v_readfirstlane_b32 s30, v149
	v_bfe_u32 v152, v0, 4, 2
	v_lshlrev_b32_e32 v153, 5, v149
	v_and_b32_e32 v153, 0x60, v153
	v_or_b32_e32 v144, v151, v150
	v_lshlrev_b32_e32 v144, 2, v144
	v_lshl_add_u32 v144, v152, 12, v144
	v_lshlrev_b32_e32 v145, 3, v150
	v_lshl_add_u32 v145, v153, 2, v145
	v_lshl_add_u32 v145, v152, 12, v145
	s_waitcnt lgkmcnt(0)
	s_cmp_lt_u32 s30, 4
	s_cselect_b32 s20, s10, s24
	s_cselect_b32 s21, s11, s25
	s_add_u32 s32, s6, 0x4000
	s_addc_u32 s33, s7, 0
	s_add_u32 s34, s6, 0x8000
	s_addc_u32 s35, s7, 0
	s_add_u32 s36, s6, 0xc000
	s_addc_u32 s37, s7, 0
	s_add_u32 s38, s20, 0x4000
	s_addc_u32 s39, s21, 0
	s_add_u32 s40, s20, 0x8000
	s_addc_u32 s41, s21, 0
	s_add_u32 s42, s20, 0xc000
	s_addc_u32 s43, s21, 0
	s_mul_hi_u32 s5, s19, 0xaaaaaaab
	s_addk_i32 s16, 0xfa
	s_lshr_b32 s10, s5, 5
	s_mov_b32 s11, 0
	global_load_dword v112, v144, s[6:7]
	global_load_dword v113, v144, s[6:7] offset:512
	global_load_dword v114, v144, s[6:7] offset:1024
	global_load_dword v115, v144, s[6:7] offset:1536
	global_load_dword v116, v144, s[6:7] offset:2048
	global_load_dword v117, v144, s[6:7] offset:2560
	global_load_dword v118, v144, s[6:7] offset:3072
	global_load_dword v119, v144, s[6:7] offset:3584
	global_load_dwordx2 v[176:177], v145, s[20:21]
	global_load_dwordx2 v[178:179], v145, s[20:21] offset:512
	global_load_dwordx2 v[180:181], v145, s[20:21] offset:1024
	global_load_dwordx2 v[182:183], v145, s[20:21] offset:1536
	global_load_dwordx2 v[184:185], v145, s[20:21] offset:2048
	global_load_dwordx2 v[186:187], v145, s[20:21] offset:2560
	global_load_dwordx2 v[188:189], v145, s[20:21] offset:3072
	global_load_dwordx2 v[190:191], v145, s[20:21] offset:3584
	global_load_dword v120, v144, s[32:33]
	global_load_dword v121, v144, s[32:33] offset:512
	global_load_dword v122, v144, s[32:33] offset:1024
	global_load_dword v123, v144, s[32:33] offset:1536
	global_load_dword v124, v144, s[32:33] offset:2048
	global_load_dword v125, v144, s[32:33] offset:2560
	global_load_dword v126, v144, s[32:33] offset:3072
	global_load_dword v127, v144, s[32:33] offset:3584
	global_load_dwordx2 v[192:193], v145, s[38:39]
	global_load_dwordx2 v[194:195], v145, s[38:39] offset:512
	global_load_dwordx2 v[196:197], v145, s[38:39] offset:1024
	global_load_dwordx2 v[198:199], v145, s[38:39] offset:1536
	global_load_dwordx2 v[200:201], v145, s[38:39] offset:2048
	global_load_dwordx2 v[202:203], v145, s[38:39] offset:2560
	global_load_dwordx2 v[204:205], v145, s[38:39] offset:3072
	global_load_dwordx2 v[206:207], v145, s[38:39] offset:3584
	s_waitcnt vmcnt(32)
	v_and_b32_e32 v242, 0xffff0000, v3
	v_lshlrev_b32_e32 v240, 3, v0
	v_sub_f32_e32 v244, v3, v242
	v_and_b32_e32 v242, 0xffff0000, v4
	v_and_b32_e32 v148, 0xf8, v240
	v_and_b32_e32 v240, 0xffff0000, v2
	v_sub_f32_e32 v245, v4, v242
	v_and_b32_e32 v242, 0xffff0000, v5
	v_sub_f32_e32 v240, v2, v240
	v_sub_f32_e32 v246, v5, v242
	v_mad_u32_u24 v247, v1, s17, v148
	v_perm_b32 v242, v3, v2, s14
	v_perm_b32 v243, v5, v4, s14
	ds_write_b64 v247, v[242:243]
	v_perm_b32 v242, v244, v240, s14
	v_perm_b32 v243, v246, v245, s14
	ds_write_b64 v247, v[242:243] offset:13056
	v_and_b32_e32 v242, 0xffff0000, v7
	v_sub_f32_e32 v244, v7, v242
	v_and_b32_e32 v242, 0xffff0000, v8
	v_and_b32_e32 v240, 0xffff0000, v6
	v_sub_f32_e32 v245, v8, v242
	v_and_b32_e32 v242, 0xffff0000, v9
	v_sub_f32_e32 v240, v6, v240
	v_sub_f32_e32 v246, v9, v242
	v_mad_u32_u24 v241, v146, s17, v148
	v_perm_b32 v242, v7, v6, s14
	v_perm_b32 v243, v9, v8, s14
	ds_write_b64 v241, v[242:243]
	v_perm_b32 v242, v244, v240, s14
	v_perm_b32 v243, v246, v245, s14
	ds_write_b64 v241, v[242:243] offset:13056
	v_and_b32_e32 v242, 0xffff0000, v11
	v_sub_f32_e32 v244, v11, v242
	v_and_b32_e32 v242, 0xffff0000, v12
	v_and_b32_e32 v240, 0xffff0000, v10
	v_sub_f32_e32 v245, v12, v242
	v_and_b32_e32 v242, 0xffff0000, v13
	v_sub_f32_e32 v240, v10, v240
	v_sub_f32_e32 v246, v13, v242
	v_perm_b32 v242, v11, v10, s14
	v_perm_b32 v243, v13, v12, s14
	ds_write_b64 v247, v[242:243] offset:8704
	v_perm_b32 v242, v244, v240, s14
	v_perm_b32 v243, v246, v245, s14
	ds_write_b64 v247, v[242:243] offset:21760
	global_load_dword v128, v144, s[34:35]
	global_load_dword v129, v144, s[34:35] offset:512
	global_load_dword v130, v144, s[34:35] offset:1024
	global_load_dword v131, v144, s[34:35] offset:1536
	global_load_dword v132, v144, s[34:35] offset:2048
	global_load_dword v133, v144, s[34:35] offset:2560
	global_load_dword v134, v144, s[34:35] offset:3072
	global_load_dword v135, v144, s[34:35] offset:3584
	global_load_dwordx2 v[208:209], v145, s[40:41]
	global_load_dwordx2 v[210:211], v145, s[40:41] offset:512
	global_load_dwordx2 v[212:213], v145, s[40:41] offset:1024
	global_load_dwordx2 v[214:215], v145, s[40:41] offset:1536
	global_load_dwordx2 v[216:217], v145, s[40:41] offset:2048
	global_load_dwordx2 v[218:219], v145, s[40:41] offset:2560
	global_load_dwordx2 v[220:221], v145, s[40:41] offset:3072
	global_load_dwordx2 v[222:223], v145, s[40:41] offset:3584
	global_load_dword v136, v144, s[36:37]
	global_load_dword v137, v144, s[36:37] offset:512
	global_load_dword v138, v144, s[36:37] offset:1024
	global_load_dword v139, v144, s[36:37] offset:1536
	global_load_dword v140, v144, s[36:37] offset:2048
	global_load_dword v141, v144, s[36:37] offset:2560
	global_load_dword v142, v144, s[36:37] offset:3072
	global_load_dword v143, v144, s[36:37] offset:3584
	global_load_dwordx2 v[224:225], v145, s[42:43]
	global_load_dwordx2 v[226:227], v145, s[42:43] offset:512
	global_load_dwordx2 v[228:229], v145, s[42:43] offset:1024
	global_load_dwordx2 v[230:231], v145, s[42:43] offset:1536
	global_load_dwordx2 v[232:233], v145, s[42:43] offset:2048
	global_load_dwordx2 v[234:235], v145, s[42:43] offset:2560
	global_load_dwordx2 v[236:237], v145, s[42:43] offset:3072
	global_load_dwordx2 v[238:239], v145, s[42:43] offset:3584
	s_waitcnt lgkmcnt(0)
	s_barrier
	s_waitcnt vmcnt(56)
	v_cvt_pk_bf16_f32 v106, v112, v113
	v_lshlrev_b32_e32 v248, 16, v106
	v_and_b32_e32 v249, 0xffff0000, v106
	v_sub_f32_e32 v248, v112, v248
	v_sub_f32_e32 v249, v113, v249
	v_cvt_pk_bf16_f32 v102, v248, v249
	v_cvt_pk_bf16_f32 v107, v114, v115
	v_lshlrev_b32_e32 v250, 16, v107
	v_and_b32_e32 v251, 0xffff0000, v107
	v_sub_f32_e32 v250, v114, v250
	v_sub_f32_e32 v251, v115, v251
	v_cvt_pk_bf16_f32 v103, v250, v251
	v_cvt_pk_bf16_f32 v108, v116, v117
	v_lshlrev_b32_e32 v248, 16, v108
	v_and_b32_e32 v249, 0xffff0000, v108
	v_sub_f32_e32 v248, v116, v248
	v_sub_f32_e32 v249, v117, v249
	v_cvt_pk_bf16_f32 v104, v248, v249
	v_cvt_pk_bf16_f32 v109, v118, v119
	v_lshlrev_b32_e32 v250, 16, v109
	v_and_b32_e32 v251, 0xffff0000, v109
	v_sub_f32_e32 v250, v118, v250
	v_sub_f32_e32 v251, v119, v251
	v_cvt_pk_bf16_f32 v105, v250, v251
	s_waitcnt vmcnt(48)
	v_cvt_pk_bf16_f32 v74, v176, v178
	v_lshlrev_b32_e32 v248, 16, v74
	v_and_b32_e32 v249, 0xffff0000, v74
	v_sub_f32_e32 v248, v176, v248
	v_sub_f32_e32 v249, v178, v249
	v_cvt_pk_bf16_f32 v70, v248, v249
	v_cvt_pk_bf16_f32 v75, v180, v182
	v_lshlrev_b32_e32 v250, 16, v75
	v_and_b32_e32 v251, 0xffff0000, v75
	v_sub_f32_e32 v250, v180, v250
	v_sub_f32_e32 v251, v182, v251
	v_cvt_pk_bf16_f32 v71, v250, v251
	v_cvt_pk_bf16_f32 v76, v184, v186
	v_lshlrev_b32_e32 v248, 16, v76
	v_and_b32_e32 v249, 0xffff0000, v76
	v_sub_f32_e32 v248, v184, v248
	v_sub_f32_e32 v249, v186, v249
	v_cvt_pk_bf16_f32 v72, v248, v249
	v_cvt_pk_bf16_f32 v77, v188, v190
	v_lshlrev_b32_e32 v250, 16, v77
	v_and_b32_e32 v251, 0xffff0000, v77
	v_sub_f32_e32 v250, v188, v250
	v_sub_f32_e32 v251, v190, v251
	v_cvt_pk_bf16_f32 v73, v250, v251
	v_cvt_pk_bf16_f32 v38, v177, v179
	v_lshlrev_b32_e32 v248, 16, v38
	v_and_b32_e32 v249, 0xffff0000, v38
	v_sub_f32_e32 v248, v177, v248
	v_sub_f32_e32 v249, v179, v249
	v_cvt_pk_bf16_f32 v42, v248, v249
	v_cvt_pk_bf16_f32 v39, v181, v183
	v_lshlrev_b32_e32 v250, 16, v39
	v_and_b32_e32 v251, 0xffff0000, v39
	v_sub_f32_e32 v250, v181, v250
	v_sub_f32_e32 v251, v183, v251
	v_cvt_pk_bf16_f32 v43, v250, v251
	v_cvt_pk_bf16_f32 v40, v185, v187
	v_lshlrev_b32_e32 v248, 16, v40
	v_and_b32_e32 v249, 0xffff0000, v40
	v_sub_f32_e32 v248, v185, v248
	v_sub_f32_e32 v249, v187, v249
	v_cvt_pk_bf16_f32 v44, v248, v249
	v_cvt_pk_bf16_f32 v41, v189, v191
	v_lshlrev_b32_e32 v250, 16, v41
	v_and_b32_e32 v251, 0xffff0000, v41
	v_sub_f32_e32 v250, v189, v250
	v_sub_f32_e32 v251, v191, v251
	v_cvt_pk_bf16_f32 v45, v250, v251
	s_waitcnt vmcnt(40)
	v_cvt_pk_bf16_f32 v98, v120, v121
	v_lshlrev_b32_e32 v248, 16, v98
	v_and_b32_e32 v249, 0xffff0000, v98
	v_sub_f32_e32 v248, v120, v248
	v_sub_f32_e32 v249, v121, v249
	v_cvt_pk_bf16_f32 v94, v248, v249
	v_cvt_pk_bf16_f32 v99, v122, v123
	v_lshlrev_b32_e32 v250, 16, v99
	v_and_b32_e32 v251, 0xffff0000, v99
	v_sub_f32_e32 v250, v122, v250
	v_sub_f32_e32 v251, v123, v251
	v_cvt_pk_bf16_f32 v95, v250, v251
	v_cvt_pk_bf16_f32 v100, v124, v125
	v_lshlrev_b32_e32 v248, 16, v100
	v_and_b32_e32 v249, 0xffff0000, v100
	v_sub_f32_e32 v248, v124, v248
	v_sub_f32_e32 v249, v125, v249
	v_cvt_pk_bf16_f32 v96, v248, v249
	v_cvt_pk_bf16_f32 v101, v126, v127
	v_lshlrev_b32_e32 v250, 16, v101
	v_and_b32_e32 v251, 0xffff0000, v101
	v_sub_f32_e32 v250, v126, v250
	v_sub_f32_e32 v251, v127, v251
	v_cvt_pk_bf16_f32 v97, v250, v251
	s_waitcnt vmcnt(32)
	v_cvt_pk_bf16_f32 v62, v192, v194
	v_lshlrev_b32_e32 v248, 16, v62
	v_and_b32_e32 v249, 0xffff0000, v62
	v_sub_f32_e32 v248, v192, v248
	v_sub_f32_e32 v249, v194, v249
	v_cvt_pk_bf16_f32 v66, v248, v249
	v_cvt_pk_bf16_f32 v63, v196, v198
	v_lshlrev_b32_e32 v250, 16, v63
	v_and_b32_e32 v251, 0xffff0000, v63
	v_sub_f32_e32 v250, v196, v250
	v_sub_f32_e32 v251, v198, v251
	v_cvt_pk_bf16_f32 v67, v250, v251
	v_cvt_pk_bf16_f32 v64, v200, v202
	v_lshlrev_b32_e32 v248, 16, v64
	v_and_b32_e32 v249, 0xffff0000, v64
	v_sub_f32_e32 v248, v200, v248
	v_sub_f32_e32 v249, v202, v249
	v_cvt_pk_bf16_f32 v68, v248, v249
	v_cvt_pk_bf16_f32 v65, v204, v206
	v_lshlrev_b32_e32 v250, 16, v65
	v_and_b32_e32 v251, 0xffff0000, v65
	v_sub_f32_e32 v250, v204, v250
	v_sub_f32_e32 v251, v206, v251
	v_cvt_pk_bf16_f32 v69, v250, v251
	v_cvt_pk_bf16_f32 v30, v193, v195
	v_lshlrev_b32_e32 v248, 16, v30
	v_and_b32_e32 v249, 0xffff0000, v30
	v_sub_f32_e32 v248, v193, v248
	v_sub_f32_e32 v249, v195, v249
	v_cvt_pk_bf16_f32 v34, v248, v249
	v_cvt_pk_bf16_f32 v31, v197, v199
	v_lshlrev_b32_e32 v250, 16, v31
	v_and_b32_e32 v251, 0xffff0000, v31
	v_sub_f32_e32 v250, v197, v250
	v_sub_f32_e32 v251, v199, v251
	v_cvt_pk_bf16_f32 v35, v250, v251
	v_cvt_pk_bf16_f32 v32, v201, v203
	v_lshlrev_b32_e32 v248, 16, v32
	v_and_b32_e32 v249, 0xffff0000, v32
	v_sub_f32_e32 v248, v201, v248
	v_sub_f32_e32 v249, v203, v249
	v_cvt_pk_bf16_f32 v36, v248, v249
	v_cvt_pk_bf16_f32 v33, v205, v207
	v_lshlrev_b32_e32 v250, 16, v33
	v_and_b32_e32 v251, 0xffff0000, v33
	v_sub_f32_e32 v250, v205, v250
	v_sub_f32_e32 v251, v207, v251
	v_cvt_pk_bf16_f32 v37, v250, v251
	s_waitcnt vmcnt(24)
	v_cvt_pk_bf16_f32 v90, v128, v129
	v_lshlrev_b32_e32 v248, 16, v90
	v_and_b32_e32 v249, 0xffff0000, v90
	v_sub_f32_e32 v248, v128, v248
	v_sub_f32_e32 v249, v129, v249
	v_cvt_pk_bf16_f32 v86, v248, v249
	v_cvt_pk_bf16_f32 v91, v130, v131
	v_lshlrev_b32_e32 v250, 16, v91
	v_and_b32_e32 v251, 0xffff0000, v91
	v_sub_f32_e32 v250, v130, v250
	v_sub_f32_e32 v251, v131, v251
	v_cvt_pk_bf16_f32 v87, v250, v251
	v_cvt_pk_bf16_f32 v92, v132, v133
	v_lshlrev_b32_e32 v248, 16, v92
	v_and_b32_e32 v249, 0xffff0000, v92
	v_sub_f32_e32 v248, v132, v248
	v_sub_f32_e32 v249, v133, v249
	v_cvt_pk_bf16_f32 v88, v248, v249
	v_cvt_pk_bf16_f32 v93, v134, v135
	v_lshlrev_b32_e32 v250, 16, v93
	v_and_b32_e32 v251, 0xffff0000, v93
	v_sub_f32_e32 v250, v134, v250
	v_sub_f32_e32 v251, v135, v251
	v_cvt_pk_bf16_f32 v89, v250, v251
	s_waitcnt vmcnt(16)
	v_cvt_pk_bf16_f32 v54, v208, v210
	v_lshlrev_b32_e32 v248, 16, v54
	v_and_b32_e32 v249, 0xffff0000, v54
	v_sub_f32_e32 v248, v208, v248
	v_sub_f32_e32 v249, v210, v249
	v_cvt_pk_bf16_f32 v58, v248, v249
	v_cvt_pk_bf16_f32 v55, v212, v214
	v_lshlrev_b32_e32 v250, 16, v55
	v_and_b32_e32 v251, 0xffff0000, v55
	v_sub_f32_e32 v250, v212, v250
	v_sub_f32_e32 v251, v214, v251
	v_cvt_pk_bf16_f32 v59, v250, v251
	v_cvt_pk_bf16_f32 v56, v216, v218
	v_lshlrev_b32_e32 v248, 16, v56
	v_and_b32_e32 v249, 0xffff0000, v56
	v_sub_f32_e32 v248, v216, v248
	v_sub_f32_e32 v249, v218, v249
	v_cvt_pk_bf16_f32 v60, v248, v249
	v_cvt_pk_bf16_f32 v57, v220, v222
	v_lshlrev_b32_e32 v250, 16, v57
	v_and_b32_e32 v251, 0xffff0000, v57
	v_sub_f32_e32 v250, v220, v250
	v_sub_f32_e32 v251, v222, v251
	v_cvt_pk_bf16_f32 v61, v250, v251
	v_cvt_pk_bf16_f32 v26, v209, v211
	v_lshlrev_b32_e32 v248, 16, v26
	v_and_b32_e32 v249, 0xffff0000, v26
	v_sub_f32_e32 v248, v209, v248
	v_sub_f32_e32 v249, v211, v249
	v_cvt_pk_bf16_f32 v22, v248, v249
	v_cvt_pk_bf16_f32 v27, v213, v215
	v_lshlrev_b32_e32 v250, 16, v27
	v_and_b32_e32 v251, 0xffff0000, v27
	v_sub_f32_e32 v250, v213, v250
	v_sub_f32_e32 v251, v215, v251
	v_cvt_pk_bf16_f32 v23, v250, v251
	v_cvt_pk_bf16_f32 v28, v217, v219
	v_lshlrev_b32_e32 v248, 16, v28
	v_and_b32_e32 v249, 0xffff0000, v28
	v_sub_f32_e32 v248, v217, v248
	v_sub_f32_e32 v249, v219, v249
	v_cvt_pk_bf16_f32 v24, v248, v249
	v_cvt_pk_bf16_f32 v29, v221, v223
	v_lshlrev_b32_e32 v250, 16, v29
	v_and_b32_e32 v251, 0xffff0000, v29
	v_sub_f32_e32 v250, v221, v250
	v_sub_f32_e32 v251, v223, v251
	v_cvt_pk_bf16_f32 v25, v250, v251
	s_waitcnt vmcnt(8)
	v_cvt_pk_bf16_f32 v82, v136, v137
	v_lshlrev_b32_e32 v248, 16, v82
	v_and_b32_e32 v249, 0xffff0000, v82
	v_sub_f32_e32 v248, v136, v248
	v_sub_f32_e32 v249, v137, v249
	v_cvt_pk_bf16_f32 v78, v248, v249
	v_cvt_pk_bf16_f32 v83, v138, v139
	v_lshlrev_b32_e32 v250, 16, v83
	v_and_b32_e32 v251, 0xffff0000, v83
	v_sub_f32_e32 v250, v138, v250
	v_sub_f32_e32 v251, v139, v251
	v_cvt_pk_bf16_f32 v79, v250, v251
	v_cvt_pk_bf16_f32 v84, v140, v141
	v_lshlrev_b32_e32 v248, 16, v84
	v_and_b32_e32 v249, 0xffff0000, v84
	v_sub_f32_e32 v248, v140, v248
	v_sub_f32_e32 v249, v141, v249
	v_cvt_pk_bf16_f32 v80, v248, v249
	v_cvt_pk_bf16_f32 v85, v142, v143
	v_lshlrev_b32_e32 v250, 16, v85
	v_and_b32_e32 v251, 0xffff0000, v85
	v_sub_f32_e32 v250, v142, v250
	v_sub_f32_e32 v251, v143, v251
	v_cvt_pk_bf16_f32 v81, v250, v251
	s_waitcnt vmcnt(0)
	v_cvt_pk_bf16_f32 v46, v224, v226
	v_lshlrev_b32_e32 v248, 16, v46
	v_and_b32_e32 v249, 0xffff0000, v46
	v_sub_f32_e32 v248, v224, v248
	v_sub_f32_e32 v249, v226, v249
	v_cvt_pk_bf16_f32 v50, v248, v249
	v_cvt_pk_bf16_f32 v47, v228, v230
	v_lshlrev_b32_e32 v250, 16, v47
	v_and_b32_e32 v251, 0xffff0000, v47
	v_sub_f32_e32 v250, v228, v250
	v_sub_f32_e32 v251, v230, v251
	v_cvt_pk_bf16_f32 v51, v250, v251
	v_cvt_pk_bf16_f32 v48, v232, v234
	v_lshlrev_b32_e32 v248, 16, v48
	v_and_b32_e32 v249, 0xffff0000, v48
	v_sub_f32_e32 v248, v232, v248
	v_sub_f32_e32 v249, v234, v249
	v_cvt_pk_bf16_f32 v52, v248, v249
	v_cvt_pk_bf16_f32 v49, v236, v238
	v_lshlrev_b32_e32 v250, 16, v49
	v_and_b32_e32 v251, 0xffff0000, v49
	v_sub_f32_e32 v250, v236, v250
	v_sub_f32_e32 v251, v238, v251
	v_cvt_pk_bf16_f32 v53, v250, v251
	v_cvt_pk_bf16_f32 v18, v225, v227
	v_lshlrev_b32_e32 v248, 16, v18
	v_and_b32_e32 v249, 0xffff0000, v18
	v_sub_f32_e32 v248, v225, v248
	v_sub_f32_e32 v249, v227, v249
	v_cvt_pk_bf16_f32 v14, v248, v249
	v_cvt_pk_bf16_f32 v19, v229, v231
	v_lshlrev_b32_e32 v250, 16, v19
	v_and_b32_e32 v251, 0xffff0000, v19
	v_sub_f32_e32 v250, v229, v250
	v_sub_f32_e32 v251, v231, v251
	v_cvt_pk_bf16_f32 v15, v250, v251
	v_cvt_pk_bf16_f32 v20, v233, v235
	v_lshlrev_b32_e32 v248, 16, v20
	v_and_b32_e32 v249, 0xffff0000, v20
	v_sub_f32_e32 v248, v233, v248
	v_sub_f32_e32 v249, v235, v249
	v_cvt_pk_bf16_f32 v16, v248, v249
	v_cvt_pk_bf16_f32 v21, v237, v239
	v_lshlrev_b32_e32 v250, 16, v21
	v_and_b32_e32 v251, 0xffff0000, v21
	v_sub_f32_e32 v250, v237, v250
	v_sub_f32_e32 v251, v239, v251
	v_cvt_pk_bf16_f32 v17, v250, v251
	v_mov_b32_e32 v113, 0
	v_cmp_gt_u32_e32 vcc, 0x100, v0
	v_and_b32_e32 v115, 63, v0
	v_lshrrev_b32_e32 v125, 2, v115
	v_lshlrev_b32_e32 v114, 2, v0
	v_and_b32_e32 v114, 12, v114
	v_mul_u32_u24_e32 v115, 20, v125
	v_mul_u32_u24_e32 v112, 0xa00, v149
	v_lshlrev_b32_e32 v115, 2, v115
	v_lshlrev_b32_e32 v120, 2, v114
	v_add3_u32 v118, v112, v115, v120
	v_lshlrev_b32_e32 v112, 2, v151
	v_lshl_add_u64 v[114:115], s[26:27], 0, v[112:113]
	v_mov_b32_e32 v112, 0x100
	v_cndmask_b32_e64 v112, v112, 0, vcc
	v_lshl_add_u64 v[122:123], s[28:29], 0, v[112:113]
	v_lshlrev_b32_e32 v112, 1, v153
	v_mov_b32_e32 v121, v113
	v_lshl_add_u64 v[112:113], v[122:123], 0, v[112:113]
	v_lshl_add_u64 v[114:115], v[114:115], 0, v[120:121]
	v_lshl_add_u64 v[112:113], v[112:113], 0, v[120:121]
	v_mul_u32_u24_e32 v120, 0x50, v152
	v_or_b32_e32 v120, v120, v150
	v_and_b32_e32 v124, 48, v0
	s_movk_i32 s4, 0xa00
	v_lshlrev_b32_e32 v120, 2, v120
	v_add_u32_e32 v122, s15, v125
	v_mul_u32_u24_e32 v116, 0x110, v1
	v_mul_u32_u24_e32 v117, 0x110, v146
	v_or_b32_e32 v119, 0xc350, v125
	s_max_u32 s6, s10, 1
	v_mad_u32_u24 v120, v149, s4, v120
	v_mad_u32_u24 v121, v150, s17, v124
	v_add_u32_e32 v122, 0xffffd887, v122
	v_add_u32_e32 v240, 0xcc00, v120
	v_add_u32_e32 v241, 0xd000, v120
	v_mov_b32_e32 v242, v119
	v_mov_b32_e32 v243, 0
	v_lshlrev_b64 v[244:245], 9, v[242:243]
	v_lshl_add_u64 v[228:229], v[114:115], 0, v[244:245]
	v_lshl_add_u64 v[230:231], v[112:113], 0, v[244:245]
	s_branch .LBB0_9

.LBB0_13:
	ds_read_b128 v[176:179], v123
	ds_read_b128 v[192:195], v123 offset:13056
	ds_read_b128 v[180:183], v123 offset:64
	ds_read_b128 v[196:199], v123 offset:13120
	ds_read_b128 v[184:187], v123 offset:128
	ds_read_b128 v[200:203], v123 offset:13184
	ds_read_b128 v[188:191], v123 offset:192
	ds_read_b128 v[204:207], v123 offset:13248
	s_add_i32 s8, s8, -1
	s_waitcnt lgkmcnt(6)
	v_mfma_f32_16x16x32_bf16 v[208:211], v[176:179], v[106:109], 0
	v_mfma_f32_16x16x32_bf16 v[212:215], v[176:179], v[74:77], 0
	v_mfma_f32_16x16x32_bf16 v[216:219], v[176:179], v[38:41], 0
	v_mfma_f32_16x16x32_bf16 v[208:211], v[192:195], v[106:109], v[208:211]
	v_mfma_f32_16x16x32_bf16 v[212:215], v[192:195], v[74:77], v[212:215]
	v_mfma_f32_16x16x32_bf16 v[216:219], v[192:195], v[38:41], v[216:219]
	v_mfma_f32_16x16x32_bf16 v[208:211], v[176:179], v[102:105], v[208:211]
	v_mfma_f32_16x16x32_bf16 v[212:215], v[176:179], v[70:73], v[212:215]
	v_mfma_f32_16x16x32_bf16 v[216:219], v[176:179], v[42:45], v[216:219]
	ds_write_b32 v120, v224 offset:53504
	ds_write2_b32 v240, v220, v221 offset1:20
	ds_write2_b32 v241, v225, v226 offset0:84 offset1:104
	ds_write2_b32 v240, v222, v223 offset0:40 offset1:60
	ds_write_b32 v120, v227 offset:53744
	ds_read_b128 v[232:235], v118 offset:52224
	ds_read_b128 v[236:239], v118 offset:53504
	v_add_u32_e32 v123, 0x1100, v123
	s_waitcnt lgkmcnt(11)
	v_mfma_f32_16x16x32_bf16 v[208:211], v[180:183], v[98:101], v[208:211]
	v_mfma_f32_16x16x32_bf16 v[212:215], v[180:183], v[62:65], v[212:215]
	v_mfma_f32_16x16x32_bf16 v[216:219], v[180:183], v[30:33], v[216:219]
	v_mfma_f32_16x16x32_bf16 v[208:211], v[196:199], v[98:101], v[208:211]
	v_mfma_f32_16x16x32_bf16 v[212:215], v[196:199], v[62:65], v[212:215]
	v_mfma_f32_16x16x32_bf16 v[216:219], v[196:199], v[30:33], v[216:219]
	v_mfma_f32_16x16x32_bf16 v[208:211], v[180:183], v[94:97], v[208:211]
	v_mfma_f32_16x16x32_bf16 v[212:215], v[180:183], v[66:69], v[212:215]
	v_mfma_f32_16x16x32_bf16 v[216:219], v[180:183], v[34:37], v[216:219]
	s_waitcnt lgkmcnt(9)
	v_mfma_f32_16x16x32_bf16 v[208:211], v[184:187], v[90:93], v[208:211]
	v_mfma_f32_16x16x32_bf16 v[212:215], v[184:187], v[54:57], v[212:215]
	v_mfma_f32_16x16x32_bf16 v[216:219], v[184:187], v[26:29], v[216:219]
	v_mfma_f32_16x16x32_bf16 v[208:211], v[200:203], v[90:93], v[208:211]
	v_mfma_f32_16x16x32_bf16 v[212:215], v[200:203], v[54:57], v[212:215]
	v_mfma_f32_16x16x32_bf16 v[216:219], v[200:203], v[26:29], v[216:219]
	v_mfma_f32_16x16x32_bf16 v[208:211], v[184:187], v[86:89], v[208:211]
	v_mfma_f32_16x16x32_bf16 v[212:215], v[184:187], v[58:61], v[212:215]
	v_mfma_f32_16x16x32_bf16 v[216:219], v[184:187], v[22:25], v[216:219]
	s_waitcnt lgkmcnt(7)
	v_mfma_f32_16x16x32_bf16 v[208:211], v[188:191], v[82:85], v[208:211]
	v_mfma_f32_16x16x32_bf16 v[212:215], v[188:191], v[46:49], v[212:215]
	v_mfma_f32_16x16x32_bf16 v[216:219], v[188:191], v[18:21], v[216:219]
	s_waitcnt lgkmcnt(0)
	global_store_dwordx4 v[228:229], v[232:235], off
	global_store_dwordx4 v[230:231], v[236:239], off
	v_mfma_f32_16x16x32_bf16 v[208:211], v[204:207], v[82:85], v[208:211]
	v_mfma_f32_16x16x32_bf16 v[212:215], v[204:207], v[46:49], v[212:215]
	v_mfma_f32_16x16x32_bf16 v[216:219], v[204:207], v[18:21], v[216:219]
	v_mfma_f32_16x16x32_bf16 v[208:211], v[188:191], v[78:81], v[208:211]
	v_mfma_f32_16x16x32_bf16 v[212:215], v[188:191], v[50:53], v[212:215]
	v_mfma_f32_16x16x32_bf16 v[216:219], v[188:191], v[14:17], v[216:219]
	v_cmp_gt_i32_e32 vcc, s12, v124
	s_cmp_eq_u32 s8, 0
	s_nop 1
	v_cndmask_b32_e32 v242, v119, v124, vcc
	v_ashrrev_i32_e32 v243, 31, v242
	v_lshlrev_b64 v[244:245], 9, v[242:243]
	v_add_u32_e32 v124, 16, v124
	v_lshl_add_u64 v[228:229], v[114:115], 0, v[244:245]
	v_lshl_add_u64 v[230:231], v[112:113], 0, v[244:245]
	v_mov_b32_e32 v220, v208
	v_mov_b32_e32 v221, v209
	v_mov_b32_e32 v222, v210
	v_mov_b32_e32 v223, v211
	v_cvt_pk_f16_f32 v224, v212, v216
	v_cvt_pk_f16_f32 v225, v213, v217
	v_cvt_pk_f16_f32 v226, v214, v218
	v_cvt_pk_f16_f32 v227, v215, v219
	s_cbranch_scc0 .LBB0_13

.Lg_drain:
	ds_write_b32 v120, v224 offset:53504
	ds_write2_b32 v240, v220, v221 offset1:20
	ds_write2_b32 v241, v225, v226 offset0:84 offset1:104
	ds_write2_b32 v240, v222, v223 offset0:40 offset1:60
	ds_write_b32 v120, v227 offset:53744
	ds_read_b128 v[232:235], v118 offset:52224
	ds_read_b128 v[236:239], v118 offset:53504
	s_waitcnt lgkmcnt(0)
	global_store_dwordx4 v[228:229], v[232:235], off
	global_store_dwordx4 v[230:231], v[236:239], off

.LBB1_17:
	s_load_dwordx2 s[26:27], s[0:1], 0x10
	s_movk_i32 s3, 0x1000
	s_and_b64 vcc, exec, s[8:9]
	v_cmp_lt_i32_e64 s[8:9], v0, v77
	s_cbranch_vccz .LBB1_40
	v_or_b32_e32 v113, 0x400, v0
	v_or_b32_e32 v114, 0x800, v0
	v_or_b32_e32 v115, 0xc00, v0
	v_mov_b32_e32 v116, 0x10c20
	v_mov_b32_e32 v117, 0x10c20
	v_mov_b32_e32 v118, 0x10c20
	v_mov_b32_e32 v119, 0x10c20
	v_add_u32_e32 v120, 256, v116
	v_add_u32_e32 v121, 256, v117
	v_add_u32_e32 v122, 256, v118
	v_add_u32_e32 v123, 256, v119
	ds_read_b32 v124, v120
	ds_read_b32 v125, v121
	ds_read_b32 v126, v122
	ds_read_b32 v127, v123
	s_waitcnt lgkmcnt(0)
	v_cmp_le_i32_e64 s[36:37], v124, v0
	v_cmp_le_i32_e64 s[38:39], v125, v113
	v_cmp_le_i32_e64 s[40:41], v126, v114
	v_cmp_le_i32_e64 s[42:43], v127, v115
	v_cndmask_b32_e64 v116, v116, v120, s[36:37]
	v_cndmask_b32_e64 v117, v117, v121, s[38:39]
	v_cndmask_b32_e64 v118, v118, v122, s[40:41]
	v_cndmask_b32_e64 v119, v119, v123, s[42:43]
	v_add_u32_e32 v120, 128, v116
	v_add_u32_e32 v121, 128, v117
	v_add_u32_e32 v122, 128, v118
	v_add_u32_e32 v123, 128, v119
	ds_read_b32 v124, v120
	ds_read_b32 v125, v121
	ds_read_b32 v126, v122
	ds_read_b32 v127, v123
	s_waitcnt lgkmcnt(0)
	v_cmp_le_i32_e64 s[36:37], v124, v0
	v_cmp_le_i32_e64 s[38:39], v125, v113
	v_cmp_le_i32_e64 s[40:41], v126, v114
	v_cmp_le_i32_e64 s[42:43], v127, v115
	v_cndmask_b32_e64 v116, v116, v120, s[36:37]
	v_cndmask_b32_e64 v117, v117, v121, s[38:39]
	v_cndmask_b32_e64 v118, v118, v122, s[40:41]
	v_cndmask_b32_e64 v119, v119, v123, s[42:43]
	v_add_u32_e32 v120, 64, v116
	v_add_u32_e32 v121, 64, v117
	v_add_u32_e32 v122, 64, v118
	v_add_u32_e32 v123, 64, v119
	ds_read_b32 v124, v120
	ds_read_b32 v125, v121
	ds_read_b32 v126, v122
	ds_read_b32 v127, v123
	s_waitcnt lgkmcnt(0)
	v_cmp_le_i32_e64 s[36:37], v124, v0
	v_cmp_le_i32_e64 s[38:39], v125, v113
	v_cmp_le_i32_e64 s[40:41], v126, v114
	v_cmp_le_i32_e64 s[42:43], v127, v115
	v_cndmask_b32_e64 v116, v116, v120, s[36:37]
	v_cndmask_b32_e64 v117, v117, v121, s[38:39]
	v_cndmask_b32_e64 v118, v118, v122, s[40:41]
	v_cndmask_b32_e64 v119, v119, v123, s[42:43]
	v_add_u32_e32 v120, 32, v116
	v_add_u32_e32 v121, 32, v117
	v_add_u32_e32 v122, 32, v118
	v_add_u32_e32 v123, 32, v119
	ds_read_b32 v124, v120
	ds_read_b32 v125, v121
	ds_read_b32 v126, v122
	ds_read_b32 v127, v123
	s_waitcnt lgkmcnt(0)
	v_cmp_le_i32_e64 s[36:37], v124, v0
	v_cmp_le_i32_e64 s[38:39], v125, v113
	v_cmp_le_i32_e64 s[40:41], v126, v114
	v_cmp_le_i32_e64 s[42:43], v127, v115
	v_cndmask_b32_e64 v116, v116, v120, s[36:37]
	v_cndmask_b32_e64 v117, v117, v121, s[38:39]
	v_cndmask_b32_e64 v118, v118, v122, s[40:41]
	v_cndmask_b32_e64 v119, v119, v123, s[42:43]
	v_add_u32_e32 v120, 16, v116
	v_add_u32_e32 v121, 16, v117
	v_add_u32_e32 v122, 16, v118
	v_add_u32_e32 v123, 16, v119
	ds_read_b32 v124, v120
	ds_read_b32 v125, v121
	ds_read_b32 v126, v122
	ds_read_b32 v127, v123
	s_waitcnt lgkmcnt(0)
	v_cmp_le_i32_e64 s[36:37], v124, v0
	v_cmp_le_i32_e64 s[38:39], v125, v113
	v_cmp_le_i32_e64 s[40:41], v126, v114
	v_cmp_le_i32_e64 s[42:43], v127, v115
	v_cndmask_b32_e64 v116, v116, v120, s[36:37]
	v_cndmask_b32_e64 v117, v117, v121, s[38:39]
	v_cndmask_b32_e64 v118, v118, v122, s[40:41]
	v_cndmask_b32_e64 v119, v119, v123, s[42:43]
	v_add_u32_e32 v120, 8, v116
	v_add_u32_e32 v121, 8, v117
	v_add_u32_e32 v122, 8, v118
	v_add_u32_e32 v123, 8, v119
	ds_read_b32 v124, v120
	ds_read_b32 v125, v121
	ds_read_b32 v126, v122
	ds_read_b32 v127, v123
	s_waitcnt lgkmcnt(0)
	v_cmp_le_i32_e64 s[36:37], v124, v0
	v_cmp_le_i32_e64 s[38:39], v125, v113
	v_cmp_le_i32_e64 s[40:41], v126, v114
	v_cmp_le_i32_e64 s[42:43], v127, v115
	v_cndmask_b32_e64 v116, v116, v120, s[36:37]
	v_cndmask_b32_e64 v117, v117, v121, s[38:39]
	v_cndmask_b32_e64 v118, v118, v122, s[40:41]
	v_cndmask_b32_e64 v119, v119, v123, s[42:43]
	v_add_u32_e32 v120, 4, v116
	v_add_u32_e32 v121, 4, v117
	v_add_u32_e32 v122, 4, v118
	v_add_u32_e32 v123, 4, v119
	ds_read_b32 v124, v120
	ds_read_b32 v125, v121
	ds_read_b32 v126, v122
	ds_read_b32 v127, v123
	s_waitcnt lgkmcnt(0)
	v_cmp_le_i32_e64 s[36:37], v124, v0
	v_cmp_le_i32_e64 s[38:39], v125, v113
	v_cmp_le_i32_e64 s[40:41], v126, v114
	v_cmp_le_i32_e64 s[42:43], v127, v115
	v_cndmask_b32_e64 v116, v116, v120, s[36:37]
	v_cndmask_b32_e64 v117, v117, v121, s[38:39]
	v_cndmask_b32_e64 v118, v118, v122, s[40:41]
	v_cndmask_b32_e64 v119, v119, v123, s[42:43]
	ds_read_b32 v120, v116
	ds_read_b32 v121, v117
	ds_read_b32 v122, v118
	ds_read_b32 v123, v119
	ds_read_b32 v124, v116 offset:528
	ds_read_b32 v125, v117 offset:528
	ds_read_b32 v126, v118 offset:528
	ds_read_b32 v127, v119 offset:528
	v_cmp_lt_i32_e64 s[10:11], v114, v77
	v_cmp_lt_i32_e64 s[12:13], v115, v77
	s_waitcnt lgkmcnt(0)
	v_add_u32_e32 v124, v124, v0
	v_add_u32_e32 v125, v125, v113
	v_add_u32_e32 v126, v126, v114
	v_add_u32_e32 v127, v127, v115
	v_sub_u32_e32 v116, v124, v120
	v_sub_u32_e32 v118, v125, v121
	v_sub_u32_e32 v120, v126, v122
	v_sub_u32_e32 v122, v127, v123
	v_ashrrev_i32_e32 v117, 31, v116
	v_ashrrev_i32_e32 v119, 31, v118
	v_ashrrev_i32_e32 v121, 31, v120
	v_ashrrev_i32_e32 v123, 31, v122
	v_lshl_add_u64 v[116:117], v[116:117], 3, s[24:25]
	v_lshl_add_u64 v[118:119], v[118:119], 3, s[24:25]
	v_lshl_add_u64 v[120:121], v[120:121], 3, s[24:25]
	v_lshl_add_u64 v[122:123], v[122:123], 3, s[24:25]
	v_cmp_lt_i32_e32 vcc, v113, v77
	s_mov_b64 s[16:17], exec
	s_and_b64 exec, s[16:17], s[8:9]
	global_load_dwordx2 v[42:43], v[116:117], off
	s_and_b64 exec, s[16:17], vcc
	global_load_dwordx2 v[44:45], v[118:119], off
	s_and_b64 exec, s[16:17], s[10:11]
	global_load_dwordx2 v[46:47], v[120:121], off
	s_and_b64 exec, s[16:17], s[12:13]
	global_load_dwordx2 v[48:49], v[122:123], off
	s_mov_b64 exec, s[16:17]
.LBB1_34:
	v_mov_b32_e32 v2, 0
	v_mov_b32_e32 v3, v2
	v_mov_b32_e32 v4, v2
	v_mov_b32_e32 v5, v2
	s_and_saveexec_b64 s[16:17], s[8:9]
	s_cbranch_execnz .LBB1_190
	s_or_b64 exec, exec, s[16:17]
	s_and_saveexec_b64 s[8:9], vcc
	s_cbranch_execnz .LBB1_191

	.amdhsa_kernel _Z11edge_kernelPK15HIP_vector_typeIjLj2EEPKiPiPS_IiLj2EEPKfPK6__halfPfSD_
		.amdhsa_group_segment_fixed_size 69680
		.amdhsa_private_segment_fixed_size 0
		.amdhsa_kernarg_size 64
		.amdhsa_user_sgpr_count 2
		.amdhsa_user_sgpr_dispatch_ptr 0
		.amdhsa_user_sgpr_queue_ptr 0
		.amdhsa_user_sgpr_kernarg_segment_ptr 1
		.amdhsa_user_sgpr_dispatch_id 0
		.amdhsa_user_sgpr_kernarg_preload_length 0
		.amdhsa_user_sgpr_kernarg_preload_offset 0
		.amdhsa_user_sgpr_private_segment_size 0
		.amdhsa_uses_dynamic_stack 0
		.amdhsa_enable_private_segment 0
		.amdhsa_system_sgpr_workgroup_id_x 1
		.amdhsa_system_sgpr_workgroup_id_y 0
		.amdhsa_system_sgpr_workgroup_id_z 0
		.amdhsa_system_sgpr_workgroup_info 0
		.amdhsa_system_vgpr_workitem_id 0
		.amdhsa_next_free_vgpr 128
		.amdhsa_next_free_sgpr 44
		.amdhsa_accum_offset 128
		.amdhsa_reserve_vcc 1
		.amdhsa_float_round_mode_32 0
		.amdhsa_float_round_mode_16_64 0
		.amdhsa_float_denorm_mode_32 3
		.amdhsa_float_denorm_mode_16_64 3
		.amdhsa_dx10_clamp 1
		.amdhsa_ieee_mode 1
		.amdhsa_fp16_overflow 0
		.amdhsa_tg_split 0
		.amdhsa_exception_fp_ieee_invalid_op 0
		.amdhsa_exception_fp_denorm_src 0
		.amdhsa_exception_fp_ieee_div_zero 0
		.amdhsa_exception_fp_ieee_overflow 0
		.amdhsa_exception_fp_ieee_underflow 0
		.amdhsa_exception_fp_ieee_inexact 0
		.amdhsa_exception_int_div_zero 0
	.end_amdhsa_kernel

amdhsa.kernels:
  - .agpr_count:     0
    .args:
      - .actual_access:  read_only
        .address_space:  global
        .offset:         0
        .size:           8
        .value_kind:     global_buffer
      - .actual_access:  read_only
        .address_space:  global
        .offset:         8
        .size:           8
        .value_kind:     global_buffer
      - .actual_access:  write_only
        .address_space:  global
        .offset:         16
        .size:           8
        .value_kind:     global_buffer
      - .actual_access:  write_only
        .address_space:  global
        .offset:         24
        .size:           8
        .value_kind:     global_buffer
      - .actual_access:  write_only
        .address_space:  global
        .offset:         32
        .size:           8
        .value_kind:     global_buffer
      - .actual_access:  read_only
        .address_space:  global
        .offset:         40
        .size:           8
        .value_kind:     global_buffer
      - .actual_access:  read_only
        .address_space:  global
        .offset:         48
        .size:           8
        .value_kind:     global_buffer
      - .actual_access:  read_only
        .address_space:  global
        .offset:         56
        .size:           8
        .value_kind:     global_buffer
      - .actual_access:  read_only
        .address_space:  global
        .offset:         64
        .size:           8
        .value_kind:     global_buffer
      - .actual_access:  write_only
        .address_space:  global
        .offset:         72
        .size:           8
        .value_kind:     global_buffer
      - .actual_access:  write_only
        .address_space:  global
        .offset:         80
        .size:           8
        .value_kind:     global_buffer
    .group_segment_fixed_size: 72704
    .kernarg_segment_align: 8
    .kernarg_segment_size: 88
    .language:       OpenCL C
    .language_version:
      - 2
      - 0
    .max_flat_workgroup_size: 512
    .name:           _Z9l1_kernelPKiS0_P15HIP_vector_typeIjLj2EEPiS4_PKfS6_S6_S6_PfP6__half
    .private_segment_fixed_size: 0
    .sgpr_count:     76
    .sgpr_spill_count: 0
    .symbol:         _Z9l1_kernelPKiS0_P15HIP_vector_typeIjLj2EEPiS4_PKfS6_S6_S6_PfP6__half.kd
    .uniform_work_group_size: 1
    .uses_dynamic_stack: false
    .vgpr_count:     252
    .vgpr_spill_count: 0
    .wavefront_size: 64
  - .agpr_count:     0
    .args:
      - .actual_access:  read_only
        .address_space:  global
        .offset:         0
        .size:           8
        .value_kind:     global_buffer
      - .actual_access:  read_only
        .address_space:  global
        .offset:         8
        .size:           8
        .value_kind:     global_buffer
      - .address_space:  global
        .offset:         16
        .size:           8
        .value_kind:     global_buffer
      - .address_space:  global
        .offset:         24
        .size:           8
        .value_kind:     global_buffer
      - .actual_access:  read_only
        .address_space:  global
        .offset:         32
        .size:           8
        .value_kind:     global_buffer
      - .actual_access:  read_only
        .address_space:  global
        .offset:         40
        .size:           8
        .value_kind:     global_buffer
      - .actual_access:  write_only
        .address_space:  global
        .offset:         48
        .size:           8
        .value_kind:     global_buffer
      - .actual_access:  write_only
        .address_space:  global
        .offset:         56
        .size:           8
        .value_kind:     global_buffer
    .group_segment_fixed_size: 69680
    .kernarg_segment_align: 8
    .kernarg_segment_size: 64
    .language:       OpenCL C
    .language_version:
      - 2
      - 0
    .max_flat_workgroup_size: 1024
    .name:           _Z11edge_kernelPK15HIP_vector_typeIjLj2EEPKiPiPS_IiLj2EEPKfPK6__halfPfSD_
    .private_segment_fixed_size: 0
    .sgpr_count:     50
    .sgpr_spill_count: 0
    .symbol:         _Z11edge_kernelPK15HIP_vector_typeIjLj2EEPKiPiPS_IiLj2EEPKfPK6__halfPfSD_.kd
    .uniform_work_group_size: 1
    .uses_dynamic_stack: false
    .vgpr_count:     128
    .vgpr_spill_count: 0
    .wavefront_size: 64
